# v19 plus priority raised only over MFMA segments in fast path, 8-deep K prefetch in layer 1
# speedup vs baseline: 1.0261x; 1.0039x over previous
.LBB0_556:
	s_cmp_le_i32 s63, s28
	s_cbranch_scc0 .Lorig_a0b0
	s_cmp_eq_u32 s17, 0
	s_cbranch_scc1 .Lorig_a0b0
	s_setprio 3
	ds_read_b128 v[116:119], v189 offset:0
	ds_read_b128 v[120:123], v226 offset:0
	ds_read_b128 v[124:127], v227 offset:0
	ds_read_b128 v[128:131], v228 offset:0
	s_waitcnt lgkmcnt(3)
	v_mfma_f32_32x32x16_bf16 v[84:99], v[116:119], v[132:135], 0
	ds_read_b128 v[116:119], v232 offset:0
	s_waitcnt lgkmcnt(3)
	v_mfma_f32_32x32x16_bf16 v[84:99], v[120:123], v[136:139], v[84:99]
	ds_read_b128 v[120:123], v233 offset:0
	s_waitcnt lgkmcnt(3)
	v_mfma_f32_32x32x16_bf16 v[84:99], v[124:127], v[140:143], v[84:99]
	ds_read_b128 v[124:127], v234 offset:0
	s_waitcnt lgkmcnt(3)
	v_mfma_f32_32x32x16_bf16 v[84:99], v[128:131], v[144:147], v[84:99]
	ds_read_b128 v[128:131], v235 offset:0
	s_waitcnt lgkmcnt(3)
	v_mfma_f32_32x32x16_bf16 v[84:99], v[116:119], v[148:151], v[84:99]
	ds_read_b128 v[116:119], v190 offset:0
	s_waitcnt lgkmcnt(3)
	v_mfma_f32_32x32x16_bf16 v[84:99], v[120:123], v[152:155], v[84:99]
	ds_read_b128 v[120:123], v229 offset:0
	s_waitcnt lgkmcnt(3)
	v_mfma_f32_32x32x16_bf16 v[84:99], v[124:127], v[156:159], v[84:99]
	ds_read_b128 v[124:127], v230 offset:0
	s_waitcnt lgkmcnt(3)
	v_mfma_f32_32x32x16_bf16 v[84:99], v[128:131], v[160:163], v[84:99]
	ds_read_b128 v[128:131], v231 offset:0
	s_waitcnt lgkmcnt(3)
	v_mfma_f32_32x32x16_bf16 v[84:99], v[116:119], v[164:167], v[84:99]
	ds_read_b128 v[116:119], v189 offset:8192
	s_waitcnt lgkmcnt(3)
	v_mfma_f32_32x32x16_bf16 v[84:99], v[120:123], v[172:175], v[84:99]
	ds_read_b128 v[120:123], v226 offset:8192
	s_waitcnt lgkmcnt(3)
	v_mfma_f32_32x32x16_bf16 v[84:99], v[124:127], v[168:171], v[84:99]
	ds_read_b128 v[124:127], v227 offset:8192
	s_waitcnt lgkmcnt(3)
	v_mfma_f32_32x32x16_bf16 v[84:99], v[128:131], v[176:179], v[84:99]
	ds_read_b128 v[128:131], v228 offset:8192
	s_waitcnt lgkmcnt(3)
	v_mfma_f32_32x32x16_bf16 v[68:83], v[116:119], v[132:135], 0
	ds_read_b128 v[116:119], v232 offset:8192
	s_waitcnt lgkmcnt(3)
	v_mfma_f32_32x32x16_bf16 v[68:83], v[120:123], v[136:139], v[68:83]
	ds_read_b128 v[120:123], v233 offset:8192
	s_waitcnt lgkmcnt(3)
	v_mfma_f32_32x32x16_bf16 v[68:83], v[124:127], v[140:143], v[68:83]
	ds_read_b128 v[124:127], v234 offset:8192
	s_waitcnt lgkmcnt(3)
	v_mfma_f32_32x32x16_bf16 v[68:83], v[128:131], v[144:147], v[68:83]
	ds_read_b128 v[128:131], v235 offset:8192
	s_waitcnt lgkmcnt(3)
	v_mfma_f32_32x32x16_bf16 v[68:83], v[116:119], v[148:151], v[68:83]
	ds_read_b128 v[116:119], v190 offset:4096
	s_waitcnt lgkmcnt(3)
	v_mfma_f32_32x32x16_bf16 v[68:83], v[120:123], v[152:155], v[68:83]
	ds_read_b128 v[120:123], v229 offset:4096
	s_waitcnt lgkmcnt(3)
	v_mfma_f32_32x32x16_bf16 v[68:83], v[124:127], v[156:159], v[68:83]
	ds_read_b128 v[124:127], v230 offset:4096
	s_waitcnt lgkmcnt(3)
	v_mfma_f32_32x32x16_bf16 v[68:83], v[128:131], v[160:163], v[68:83]
	ds_read_b128 v[128:131], v231 offset:4096
	s_waitcnt lgkmcnt(3)
	v_mfma_f32_32x32x16_bf16 v[68:83], v[116:119], v[164:167], v[68:83]
	s_waitcnt lgkmcnt(2)
	v_mfma_f32_32x32x16_bf16 v[68:83], v[120:123], v[172:175], v[68:83]
	s_waitcnt lgkmcnt(1)
	v_mfma_f32_32x32x16_bf16 v[68:83], v[124:127], v[168:171], v[68:83]
	s_waitcnt lgkmcnt(0)
	v_mfma_f32_32x32x16_bf16 v[68:83], v[128:131], v[176:179], v[68:83]
	ds_read_b64_tr_b16 v[116:117], v191 offset:0
	ds_read_b64_tr_b16 v[118:119], v191 offset:2048
	ds_read_b64_tr_b16 v[120:121], v191 offset:4096
	ds_read_b64_tr_b16 v[122:123], v191 offset:6144
	ds_read_b64_tr_b16 v[124:125], v191 offset:8192
	ds_read_b64_tr_b16 v[126:127], v191 offset:10240
	ds_read_b64_tr_b16 v[128:129], v191 offset:12288
	ds_read_b64_tr_b16 v[130:131], v191 offset:14336
	s_setprio 0
	s_nop 7
	s_nop 3
	v_cmp_eq_f32_e32 vcc, 0, v223
	s_cmp_eq_u64 vcc, exec
	s_cbranch_scc0 .Lsub_a0b0
	v_exp_f32_e32 v100, v84
	v_exp_f32_e32 v101, v85
	v_exp_f32_e32 v102, v86
	v_exp_f32_e32 v103, v87
	v_exp_f32_e32 v104, v88
	v_exp_f32_e32 v105, v89
	v_exp_f32_e32 v106, v90
	v_exp_f32_e32 v107, v91
	v_exp_f32_e32 v108, v92
	v_exp_f32_e32 v109, v93
	v_exp_f32_e32 v110, v94
	v_exp_f32_e32 v111, v95
	v_exp_f32_e32 v112, v96
	v_exp_f32_e32 v113, v97
	v_exp_f32_e32 v114, v98
	v_exp_f32_e32 v115, v99
	v_add_f32_e32 v237, v100, v101
	v_add_f32_e32 v251, v102, v103
	v_add_f32_e32 v237, v237, v104
	v_add_f32_e32 v251, v251, v105
	v_add_f32_e32 v237, v237, v106
	v_add_f32_e32 v251, v251, v107
	v_add_f32_e32 v237, v237, v108
	v_add_f32_e32 v251, v251, v109
	v_add_f32_e32 v237, v237, v110
	v_add_f32_e32 v251, v251, v111
	v_add_f32_e32 v237, v237, v112
	v_add_f32_e32 v251, v251, v113
	v_add_f32_e32 v237, v237, v114
	v_add_f32_e32 v251, v251, v115
	v_add_f32_e32 v237, v237, v251
	v_cvt_pk_bf16_f32 v238, v100, v101
	v_cvt_pk_bf16_f32 v239, v102, v103
	v_cvt_pk_bf16_f32 v240, v104, v105
	v_cvt_pk_bf16_f32 v241, v106, v107
	v_cvt_pk_bf16_f32 v242, v108, v109
	v_cvt_pk_bf16_f32 v243, v110, v111
	v_cvt_pk_bf16_f32 v244, v112, v113
	v_cvt_pk_bf16_f32 v245, v114, v115
	s_nop 1
	v_permlane32_swap_b32_e32 v238, v240
	v_permlane32_swap_b32_e32 v239, v241
	v_permlane32_swap_b32_e32 v242, v244
	v_permlane32_swap_b32_e32 v243, v245
	v_exp_f32_e32 v100, v68
	v_exp_f32_e32 v101, v69
	v_exp_f32_e32 v102, v70
	v_exp_f32_e32 v103, v71
	v_exp_f32_e32 v104, v72
	v_exp_f32_e32 v105, v73
	v_exp_f32_e32 v106, v74
	v_exp_f32_e32 v107, v75
	v_exp_f32_e32 v108, v76
	v_exp_f32_e32 v109, v77
	v_exp_f32_e32 v110, v78
	v_exp_f32_e32 v111, v79
	v_exp_f32_e32 v112, v80
	v_exp_f32_e32 v113, v81
	v_exp_f32_e32 v114, v82
	v_exp_f32_e32 v115, v83
	v_add_f32_e32 v250, v100, v101
	v_add_f32_e32 v251, v102, v103
	v_add_f32_e32 v250, v250, v104
	v_add_f32_e32 v251, v251, v105
	v_add_f32_e32 v250, v250, v106
	v_add_f32_e32 v251, v251, v107
	v_add_f32_e32 v250, v250, v108
	v_add_f32_e32 v251, v251, v109
	v_add_f32_e32 v250, v250, v110
	v_add_f32_e32 v251, v251, v111
	v_add_f32_e32 v250, v250, v112
	v_add_f32_e32 v251, v251, v113
	v_add_f32_e32 v250, v250, v114
	v_add_f32_e32 v251, v251, v115
	v_add_f32_e32 v250, v250, v251
	v_cvt_pk_bf16_f32 v100, v100, v101
	v_cvt_pk_bf16_f32 v101, v102, v103
	v_cvt_pk_bf16_f32 v102, v104, v105
	v_cvt_pk_bf16_f32 v103, v106, v107
	v_cvt_pk_bf16_f32 v104, v108, v109
	v_cvt_pk_bf16_f32 v105, v110, v111
	v_cvt_pk_bf16_f32 v106, v112, v113
	v_cvt_pk_bf16_f32 v107, v114, v115
	s_nop 1
	v_permlane32_swap_b32_e32 v100, v102
	v_permlane32_swap_b32_e32 v101, v103
	v_permlane32_swap_b32_e32 v104, v106
	v_permlane32_swap_b32_e32 v105, v107
	s_branch .Lsum_a0b0

.Lsum_a0b0:
	v_add_f32_e32 v237, v237, v250
	v_cmp_gt_f32_e32 vcc, 0x5f800000, v237
	s_cmp_eq_u64 vcc, exec
	s_cbranch_scc0 .Lfb_a0b0
	v_mov_b32_e32 v250, v237
	s_nop 1
	v_permlane32_swap_b32_e32 v237, v250
	v_add_f32_e32 v237, v237, v250
	v_add_f32_e32 v221, v237, v221
	v_mov_b32_e32 v222, v223
	s_setprio 3
	s_waitcnt lgkmcnt(6)
	v_mfma_f32_32x32x16_bf16 v[52:67], v[116:119], v[238:241], v[52:67]
	ds_read_b64_tr_b16 v[116:117], v191 offset:512
	ds_read_b64_tr_b16 v[118:119], v191 offset:2560
	s_waitcnt lgkmcnt(6)
	v_mfma_f32_32x32x16_bf16 v[52:67], v[120:123], v[242:245], v[52:67]
	ds_read_b64_tr_b16 v[120:121], v191 offset:4608
	ds_read_b64_tr_b16 v[122:123], v191 offset:6656
	s_waitcnt lgkmcnt(6)
	v_mfma_f32_32x32x16_bf16 v[52:67], v[124:127], v[100:103], v[52:67]
	ds_read_b64_tr_b16 v[124:125], v191 offset:8704
	ds_read_b64_tr_b16 v[126:127], v191 offset:10752
	s_waitcnt lgkmcnt(6)
	v_mfma_f32_32x32x16_bf16 v[52:67], v[128:131], v[104:107], v[52:67]
	ds_read_b64_tr_b16 v[128:129], v191 offset:12800
	ds_read_b64_tr_b16 v[130:131], v191 offset:14848
	s_waitcnt lgkmcnt(6)
	v_mfma_f32_32x32x16_bf16 v[36:51], v[116:119], v[238:241], v[36:51]
	ds_read_b64_tr_b16 v[116:117], v191 offset:1024
	ds_read_b64_tr_b16 v[118:119], v191 offset:3072
	s_waitcnt lgkmcnt(6)
	v_mfma_f32_32x32x16_bf16 v[36:51], v[120:123], v[242:245], v[36:51]
	ds_read_b64_tr_b16 v[120:121], v191 offset:5120
	ds_read_b64_tr_b16 v[122:123], v191 offset:7168
	s_waitcnt lgkmcnt(6)
	v_mfma_f32_32x32x16_bf16 v[36:51], v[124:127], v[100:103], v[36:51]
	ds_read_b64_tr_b16 v[124:125], v191 offset:9216
	ds_read_b64_tr_b16 v[126:127], v191 offset:11264
	s_waitcnt lgkmcnt(6)
	v_mfma_f32_32x32x16_bf16 v[36:51], v[128:131], v[104:107], v[36:51]
	ds_read_b64_tr_b16 v[128:129], v191 offset:13312
	ds_read_b64_tr_b16 v[130:131], v191 offset:15360
	s_waitcnt lgkmcnt(6)
	v_mfma_f32_32x32x16_bf16 v[20:35], v[116:119], v[238:241], v[20:35]
	ds_read_b64_tr_b16 v[116:117], v191 offset:1536
	ds_read_b64_tr_b16 v[118:119], v191 offset:3584
	s_waitcnt lgkmcnt(6)
	v_mfma_f32_32x32x16_bf16 v[20:35], v[120:123], v[242:245], v[20:35]
	ds_read_b64_tr_b16 v[120:121], v191 offset:5632
	ds_read_b64_tr_b16 v[122:123], v191 offset:7680
	s_waitcnt lgkmcnt(6)
	v_mfma_f32_32x32x16_bf16 v[20:35], v[124:127], v[100:103], v[20:35]
	ds_read_b64_tr_b16 v[124:125], v191 offset:9728
	ds_read_b64_tr_b16 v[126:127], v191 offset:11776
	s_waitcnt lgkmcnt(6)
	v_mfma_f32_32x32x16_bf16 v[20:35], v[128:131], v[104:107], v[20:35]
	ds_read_b64_tr_b16 v[128:129], v191 offset:13824
	ds_read_b64_tr_b16 v[130:131], v191 offset:15872
	s_waitcnt lgkmcnt(6)
	v_mfma_f32_32x32x16_bf16 v[4:19], v[116:119], v[238:241], v[4:19]
	s_waitcnt lgkmcnt(4)
	v_mfma_f32_32x32x16_bf16 v[4:19], v[120:123], v[242:245], v[4:19]
	s_waitcnt lgkmcnt(2)
	v_mfma_f32_32x32x16_bf16 v[4:19], v[124:127], v[100:103], v[4:19]
	s_waitcnt lgkmcnt(0)
	v_mfma_f32_32x32x16_bf16 v[4:19], v[128:131], v[104:107], v[4:19]
	s_setprio 0
	s_branch .Ltail2_a0b0

.LBB0_571:
	s_add_i32 s98, s63, 64
	s_cmp_le_i32 s98, s28
	s_cbranch_scc0 .Lorig_a0b1
	s_setprio 3
	ds_read_b128 v[116:119], v189 offset:24576
	ds_read_b128 v[120:123], v226 offset:24576
	ds_read_b128 v[124:127], v227 offset:24576
	ds_read_b128 v[128:131], v228 offset:24576
	s_waitcnt lgkmcnt(3)
	v_mfma_f32_32x32x16_bf16 v[84:99], v[116:119], v[132:135], 0
	ds_read_b128 v[116:119], v232 offset:24576
	s_waitcnt lgkmcnt(3)
	v_mfma_f32_32x32x16_bf16 v[84:99], v[120:123], v[136:139], v[84:99]
	ds_read_b128 v[120:123], v233 offset:24576
	s_waitcnt lgkmcnt(3)
	v_mfma_f32_32x32x16_bf16 v[84:99], v[124:127], v[140:143], v[84:99]
	ds_read_b128 v[124:127], v234 offset:24576
	s_waitcnt lgkmcnt(3)
	v_mfma_f32_32x32x16_bf16 v[84:99], v[128:131], v[144:147], v[84:99]
	ds_read_b128 v[128:131], v235 offset:24576
	s_waitcnt lgkmcnt(3)
	v_mfma_f32_32x32x16_bf16 v[84:99], v[116:119], v[148:151], v[84:99]
	ds_read_b128 v[116:119], v190 offset:24576
	s_waitcnt lgkmcnt(3)
	v_mfma_f32_32x32x16_bf16 v[84:99], v[120:123], v[152:155], v[84:99]
	ds_read_b128 v[120:123], v229 offset:24576
	s_waitcnt lgkmcnt(3)
	v_mfma_f32_32x32x16_bf16 v[84:99], v[124:127], v[156:159], v[84:99]
	ds_read_b128 v[124:127], v230 offset:24576
	s_waitcnt lgkmcnt(3)
	v_mfma_f32_32x32x16_bf16 v[84:99], v[128:131], v[160:163], v[84:99]
	ds_read_b128 v[128:131], v231 offset:24576
	s_waitcnt lgkmcnt(3)
	v_mfma_f32_32x32x16_bf16 v[84:99], v[116:119], v[164:167], v[84:99]
	ds_read_b128 v[116:119], v189 offset:32768
	s_waitcnt lgkmcnt(3)
	v_mfma_f32_32x32x16_bf16 v[84:99], v[120:123], v[172:175], v[84:99]
	ds_read_b128 v[120:123], v226 offset:32768
	s_waitcnt lgkmcnt(3)
	v_mfma_f32_32x32x16_bf16 v[84:99], v[124:127], v[168:171], v[84:99]
	ds_read_b128 v[124:127], v227 offset:32768
	s_waitcnt lgkmcnt(3)
	v_mfma_f32_32x32x16_bf16 v[84:99], v[128:131], v[176:179], v[84:99]
	ds_read_b128 v[128:131], v228 offset:32768
	s_waitcnt lgkmcnt(3)
	v_mfma_f32_32x32x16_bf16 v[68:83], v[116:119], v[132:135], 0
	ds_read_b128 v[116:119], v232 offset:32768
	s_waitcnt lgkmcnt(3)
	v_mfma_f32_32x32x16_bf16 v[68:83], v[120:123], v[136:139], v[68:83]
	ds_read_b128 v[120:123], v233 offset:32768
	s_waitcnt lgkmcnt(3)
	v_mfma_f32_32x32x16_bf16 v[68:83], v[124:127], v[140:143], v[68:83]
	ds_read_b128 v[124:127], v234 offset:32768
	s_waitcnt lgkmcnt(3)
	v_mfma_f32_32x32x16_bf16 v[68:83], v[128:131], v[144:147], v[68:83]
	ds_read_b128 v[128:131], v235 offset:32768
	s_waitcnt lgkmcnt(3)
	v_mfma_f32_32x32x16_bf16 v[68:83], v[116:119], v[148:151], v[68:83]
	ds_read_b128 v[116:119], v190 offset:28672
	s_waitcnt lgkmcnt(3)
	v_mfma_f32_32x32x16_bf16 v[68:83], v[120:123], v[152:155], v[68:83]
	ds_read_b128 v[120:123], v229 offset:28672
	s_waitcnt lgkmcnt(3)
	v_mfma_f32_32x32x16_bf16 v[68:83], v[124:127], v[156:159], v[68:83]
	ds_read_b128 v[124:127], v230 offset:28672
	s_waitcnt lgkmcnt(3)
	v_mfma_f32_32x32x16_bf16 v[68:83], v[128:131], v[160:163], v[68:83]
	ds_read_b128 v[128:131], v231 offset:28672
	s_waitcnt lgkmcnt(3)
	v_mfma_f32_32x32x16_bf16 v[68:83], v[116:119], v[164:167], v[68:83]
	s_waitcnt lgkmcnt(2)
	v_mfma_f32_32x32x16_bf16 v[68:83], v[120:123], v[172:175], v[68:83]
	s_waitcnt lgkmcnt(1)
	v_mfma_f32_32x32x16_bf16 v[68:83], v[124:127], v[168:171], v[68:83]
	s_waitcnt lgkmcnt(0)
	v_mfma_f32_32x32x16_bf16 v[68:83], v[128:131], v[176:179], v[68:83]
	ds_read_b64_tr_b16 v[116:117], v191 offset:16384
	ds_read_b64_tr_b16 v[118:119], v191 offset:18432
	ds_read_b64_tr_b16 v[120:121], v191 offset:20480
	ds_read_b64_tr_b16 v[122:123], v191 offset:22528
	ds_read_b64_tr_b16 v[124:125], v191 offset:24576
	ds_read_b64_tr_b16 v[126:127], v191 offset:26624
	ds_read_b64_tr_b16 v[128:129], v191 offset:28672
	ds_read_b64_tr_b16 v[130:131], v191 offset:30720
	s_setprio 0
	s_nop 7
	s_nop 3
	v_cmp_eq_f32_e32 vcc, 0, v222
	s_cmp_eq_u64 vcc, exec
	s_cbranch_scc0 .Lsub_a0b1
	v_exp_f32_e32 v100, v84
	v_exp_f32_e32 v101, v85
	v_exp_f32_e32 v102, v86
	v_exp_f32_e32 v103, v87
	v_exp_f32_e32 v104, v88
	v_exp_f32_e32 v105, v89
	v_exp_f32_e32 v106, v90
	v_exp_f32_e32 v107, v91
	v_exp_f32_e32 v108, v92
	v_exp_f32_e32 v109, v93
	v_exp_f32_e32 v110, v94
	v_exp_f32_e32 v111, v95
	v_exp_f32_e32 v112, v96
	v_exp_f32_e32 v113, v97
	v_exp_f32_e32 v114, v98
	v_exp_f32_e32 v115, v99
	v_add_f32_e32 v237, v100, v101
	v_add_f32_e32 v251, v102, v103
	v_add_f32_e32 v237, v237, v104
	v_add_f32_e32 v251, v251, v105
	v_add_f32_e32 v237, v237, v106
	v_add_f32_e32 v251, v251, v107
	v_add_f32_e32 v237, v237, v108
	v_add_f32_e32 v251, v251, v109
	v_add_f32_e32 v237, v237, v110
	v_add_f32_e32 v251, v251, v111
	v_add_f32_e32 v237, v237, v112
	v_add_f32_e32 v251, v251, v113
	v_add_f32_e32 v237, v237, v114
	v_add_f32_e32 v251, v251, v115
	v_add_f32_e32 v237, v237, v251
	v_cvt_pk_bf16_f32 v238, v100, v101
	v_cvt_pk_bf16_f32 v239, v102, v103
	v_cvt_pk_bf16_f32 v240, v104, v105
	v_cvt_pk_bf16_f32 v241, v106, v107
	v_cvt_pk_bf16_f32 v242, v108, v109
	v_cvt_pk_bf16_f32 v243, v110, v111
	v_cvt_pk_bf16_f32 v244, v112, v113
	v_cvt_pk_bf16_f32 v245, v114, v115
	s_nop 1
	v_permlane32_swap_b32_e32 v238, v240
	v_permlane32_swap_b32_e32 v239, v241
	v_permlane32_swap_b32_e32 v242, v244
	v_permlane32_swap_b32_e32 v243, v245
	v_exp_f32_e32 v100, v68
	v_exp_f32_e32 v101, v69
	v_exp_f32_e32 v102, v70
	v_exp_f32_e32 v103, v71
	v_exp_f32_e32 v104, v72
	v_exp_f32_e32 v105, v73
	v_exp_f32_e32 v106, v74
	v_exp_f32_e32 v107, v75
	v_exp_f32_e32 v108, v76
	v_exp_f32_e32 v109, v77
	v_exp_f32_e32 v110, v78
	v_exp_f32_e32 v111, v79
	v_exp_f32_e32 v112, v80
	v_exp_f32_e32 v113, v81
	v_exp_f32_e32 v114, v82
	v_exp_f32_e32 v115, v83
	v_add_f32_e32 v250, v100, v101
	v_add_f32_e32 v251, v102, v103
	v_add_f32_e32 v250, v250, v104
	v_add_f32_e32 v251, v251, v105
	v_add_f32_e32 v250, v250, v106
	v_add_f32_e32 v251, v251, v107
	v_add_f32_e32 v250, v250, v108
	v_add_f32_e32 v251, v251, v109
	v_add_f32_e32 v250, v250, v110
	v_add_f32_e32 v251, v251, v111
	v_add_f32_e32 v250, v250, v112
	v_add_f32_e32 v251, v251, v113
	v_add_f32_e32 v250, v250, v114
	v_add_f32_e32 v251, v251, v115
	v_add_f32_e32 v250, v250, v251
	v_cvt_pk_bf16_f32 v100, v100, v101
	v_cvt_pk_bf16_f32 v101, v102, v103
	v_cvt_pk_bf16_f32 v102, v104, v105
	v_cvt_pk_bf16_f32 v103, v106, v107
	v_cvt_pk_bf16_f32 v104, v108, v109
	v_cvt_pk_bf16_f32 v105, v110, v111
	v_cvt_pk_bf16_f32 v106, v112, v113
	v_cvt_pk_bf16_f32 v107, v114, v115
	s_nop 1
	v_permlane32_swap_b32_e32 v100, v102
	v_permlane32_swap_b32_e32 v101, v103
	v_permlane32_swap_b32_e32 v104, v106
	v_permlane32_swap_b32_e32 v105, v107
	s_branch .Lsum_a0b1

.Lsum_a0b1:
	v_add_f32_e32 v237, v237, v250
	v_cmp_gt_f32_e32 vcc, 0x5f800000, v237
	s_cmp_eq_u64 vcc, exec
	s_cbranch_scc0 .Lfb_a0b1
	v_mov_b32_e32 v250, v237
	s_nop 1
	v_permlane32_swap_b32_e32 v237, v250
	v_add_f32_e32 v237, v237, v250
	v_add_f32_e32 v221, v237, v221
	v_mov_b32_e32 v223, v222
	s_setprio 3
	s_waitcnt lgkmcnt(6)
	v_mfma_f32_32x32x16_bf16 v[52:67], v[116:119], v[238:241], v[52:67]
	ds_read_b64_tr_b16 v[116:117], v191 offset:16896
	ds_read_b64_tr_b16 v[118:119], v191 offset:18944
	s_waitcnt lgkmcnt(6)
	v_mfma_f32_32x32x16_bf16 v[52:67], v[120:123], v[242:245], v[52:67]
	ds_read_b64_tr_b16 v[120:121], v191 offset:20992
	ds_read_b64_tr_b16 v[122:123], v191 offset:23040
	s_waitcnt lgkmcnt(6)
	v_mfma_f32_32x32x16_bf16 v[52:67], v[124:127], v[100:103], v[52:67]
	ds_read_b64_tr_b16 v[124:125], v191 offset:25088
	ds_read_b64_tr_b16 v[126:127], v191 offset:27136
	s_waitcnt lgkmcnt(6)
	v_mfma_f32_32x32x16_bf16 v[52:67], v[128:131], v[104:107], v[52:67]
	ds_read_b64_tr_b16 v[128:129], v191 offset:29184
	ds_read_b64_tr_b16 v[130:131], v191 offset:31232
	s_waitcnt lgkmcnt(6)
	v_mfma_f32_32x32x16_bf16 v[36:51], v[116:119], v[238:241], v[36:51]
	ds_read_b64_tr_b16 v[116:117], v191 offset:17408
	ds_read_b64_tr_b16 v[118:119], v191 offset:19456
	s_waitcnt lgkmcnt(6)
	v_mfma_f32_32x32x16_bf16 v[36:51], v[120:123], v[242:245], v[36:51]
	ds_read_b64_tr_b16 v[120:121], v191 offset:21504
	ds_read_b64_tr_b16 v[122:123], v191 offset:23552
	s_waitcnt lgkmcnt(6)
	v_mfma_f32_32x32x16_bf16 v[36:51], v[124:127], v[100:103], v[36:51]
	ds_read_b64_tr_b16 v[124:125], v191 offset:25600
	ds_read_b64_tr_b16 v[126:127], v191 offset:27648
	s_waitcnt lgkmcnt(6)
	v_mfma_f32_32x32x16_bf16 v[36:51], v[128:131], v[104:107], v[36:51]
	ds_read_b64_tr_b16 v[128:129], v191 offset:29696
	ds_read_b64_tr_b16 v[130:131], v191 offset:31744
	s_waitcnt lgkmcnt(6)
	v_mfma_f32_32x32x16_bf16 v[20:35], v[116:119], v[238:241], v[20:35]
	ds_read_b64_tr_b16 v[116:117], v191 offset:17920
	ds_read_b64_tr_b16 v[118:119], v191 offset:19968
	s_waitcnt lgkmcnt(6)
	v_mfma_f32_32x32x16_bf16 v[20:35], v[120:123], v[242:245], v[20:35]
	ds_read_b64_tr_b16 v[120:121], v191 offset:22016
	ds_read_b64_tr_b16 v[122:123], v191 offset:24064
	s_waitcnt lgkmcnt(6)
	v_mfma_f32_32x32x16_bf16 v[20:35], v[124:127], v[100:103], v[20:35]
	ds_read_b64_tr_b16 v[124:125], v191 offset:26112
	ds_read_b64_tr_b16 v[126:127], v191 offset:28160
	s_waitcnt lgkmcnt(6)
	v_mfma_f32_32x32x16_bf16 v[20:35], v[128:131], v[104:107], v[20:35]
	ds_read_b64_tr_b16 v[128:129], v191 offset:30208
	ds_read_b64_tr_b16 v[130:131], v191 offset:32256
	s_waitcnt lgkmcnt(6)
	v_mfma_f32_32x32x16_bf16 v[4:19], v[116:119], v[238:241], v[4:19]
	s_waitcnt lgkmcnt(4)
	v_mfma_f32_32x32x16_bf16 v[4:19], v[120:123], v[242:245], v[4:19]
	s_waitcnt lgkmcnt(2)
	v_mfma_f32_32x32x16_bf16 v[4:19], v[124:127], v[100:103], v[4:19]
	s_waitcnt lgkmcnt(0)
	v_mfma_f32_32x32x16_bf16 v[4:19], v[128:131], v[104:107], v[4:19]
	s_setprio 0
	s_branch .Ltail2_a0b1

.LBB0_1452:
	s_cmp_le_i32 s18, s40
	s_cbranch_scc0 .Lorig_a1b0
	s_cmp_eq_u32 s71, 0
	s_cbranch_scc1 .Lorig_a1b0
	s_setprio 3
	ds_read_b128 v[140:143], v176
	ds_read_b128 v[144:147], v176 offset:32
	ds_read_b128 v[148:151], v176 offset:64
	ds_read_b128 v[152:155], v176 offset:96
	ds_read_b128 v[208:211], v172 offset:32768
	ds_read_b128 v[212:215], v206 offset:32768
	ds_read_b128 v[216:219], v207 offset:32768
	ds_read_b128 v[220:223], v237 offset:32768
	ds_read_b128 v[224:227], v244 offset:32768
	ds_read_b128 v[228:231], v245 offset:32768
	ds_read_b128 v[232:235], v246 offset:32768
	ds_read_b128 v[238:241], v247 offset:32768
	ds_read_b128 v[156:159], v176 offset:128
	ds_read_b128 v[160:163], v176 offset:160
	ds_read_b128 v[164:167], v176 offset:192
	ds_read_b128 v[168:171], v176 offset:224
	s_waitcnt lgkmcnt(11)
	v_mfma_f32_32x32x16_bf16 v[84:99], v[208:211], v[100:103], v[140:155]
	ds_read_b128 v[208:211], v172 offset:40960
	s_waitcnt lgkmcnt(11)
	v_mfma_f32_32x32x16_bf16 v[84:99], v[212:215], v[104:107], v[84:99]
	ds_read_b128 v[212:215], v206 offset:40960
	s_waitcnt lgkmcnt(11)
	v_mfma_f32_32x32x16_bf16 v[84:99], v[216:219], v[108:111], v[84:99]
	ds_read_b128 v[216:219], v207 offset:40960
	s_waitcnt lgkmcnt(11)
	v_mfma_f32_32x32x16_bf16 v[84:99], v[220:223], v[112:115], v[84:99]
	ds_read_b128 v[220:223], v237 offset:40960
	s_waitcnt lgkmcnt(11)
	v_mfma_f32_32x32x16_bf16 v[84:99], v[224:227], v[116:119], v[84:99]
	ds_read_b128 v[224:227], v244 offset:40960
	s_waitcnt lgkmcnt(11)
	v_mfma_f32_32x32x16_bf16 v[84:99], v[228:231], v[120:123], v[84:99]
	ds_read_b128 v[228:231], v245 offset:40960
	s_waitcnt lgkmcnt(11)
	v_mfma_f32_32x32x16_bf16 v[84:99], v[232:235], v[124:127], v[84:99]
	ds_read_b128 v[232:235], v246 offset:40960
	s_waitcnt lgkmcnt(11)
	v_mfma_f32_32x32x16_bf16 v[84:99], v[238:241], v[128:131], v[84:99]
	ds_read_b128 v[238:241], v247 offset:40960
	s_waitcnt lgkmcnt(7)
	v_mfma_f32_32x32x16_bf16 v[68:83], v[208:211], v[100:103], v[156:171]
	s_waitcnt lgkmcnt(6)
	v_mfma_f32_32x32x16_bf16 v[68:83], v[212:215], v[104:107], v[68:83]
	s_waitcnt lgkmcnt(5)
	v_mfma_f32_32x32x16_bf16 v[68:83], v[216:219], v[108:111], v[68:83]
	s_waitcnt lgkmcnt(4)
	v_mfma_f32_32x32x16_bf16 v[68:83], v[220:223], v[112:115], v[68:83]
	s_waitcnt lgkmcnt(3)
	v_mfma_f32_32x32x16_bf16 v[68:83], v[224:227], v[116:119], v[68:83]
	s_waitcnt lgkmcnt(2)
	v_mfma_f32_32x32x16_bf16 v[68:83], v[228:231], v[120:123], v[68:83]
	s_waitcnt lgkmcnt(1)
	v_mfma_f32_32x32x16_bf16 v[68:83], v[232:235], v[124:127], v[68:83]
	s_waitcnt lgkmcnt(0)
	v_mfma_f32_32x32x16_bf16 v[68:83], v[238:241], v[128:131], v[68:83]
	ds_read_b64_tr_b16 v[208:209], v174 offset:0
	ds_read_b64_tr_b16 v[210:211], v174 offset:2048
	ds_read_b64_tr_b16 v[212:213], v174 offset:4096
	ds_read_b64_tr_b16 v[214:215], v174 offset:6144
	ds_read_b64_tr_b16 v[216:217], v174 offset:8192
	ds_read_b64_tr_b16 v[218:219], v174 offset:10240
	ds_read_b64_tr_b16 v[220:221], v174 offset:12288
	ds_read_b64_tr_b16 v[222:223], v174 offset:14336
	s_setprio 0
	s_nop 7
	s_nop 3
	v_cmp_eq_f32_e32 vcc, 0, v193
	s_cmp_eq_u64 vcc, exec
	s_cbranch_scc0 .Lsub_a1b0
	v_exp_f32_e32 v140, v84
	v_exp_f32_e32 v141, v85
	v_exp_f32_e32 v142, v86
	v_exp_f32_e32 v143, v87
	v_exp_f32_e32 v144, v88
	v_exp_f32_e32 v145, v89
	v_exp_f32_e32 v146, v90
	v_exp_f32_e32 v147, v91
	v_exp_f32_e32 v148, v92
	v_exp_f32_e32 v149, v93
	v_exp_f32_e32 v150, v94
	v_exp_f32_e32 v151, v95
	v_exp_f32_e32 v152, v96
	v_exp_f32_e32 v153, v97
	v_exp_f32_e32 v154, v98
	v_exp_f32_e32 v155, v99
	v_add_f32_e32 v248, v140, v141
	v_add_f32_e32 v250, v142, v143
	v_add_f32_e32 v248, v248, v144
	v_add_f32_e32 v250, v250, v145
	v_add_f32_e32 v248, v248, v146
	v_add_f32_e32 v250, v250, v147
	v_add_f32_e32 v248, v248, v148
	v_add_f32_e32 v250, v250, v149
	v_add_f32_e32 v248, v248, v150
	v_add_f32_e32 v250, v250, v151
	v_add_f32_e32 v248, v248, v152
	v_add_f32_e32 v250, v250, v153
	v_add_f32_e32 v248, v248, v154
	v_add_f32_e32 v250, v250, v155
	v_add_f32_e32 v248, v248, v250
	v_cvt_pk_bf16_f32 v140, v140, v141
	v_cvt_pk_bf16_f32 v141, v142, v143
	v_cvt_pk_bf16_f32 v142, v144, v145
	v_cvt_pk_bf16_f32 v143, v146, v147
	v_cvt_pk_bf16_f32 v144, v148, v149
	v_cvt_pk_bf16_f32 v145, v150, v151
	v_cvt_pk_bf16_f32 v146, v152, v153
	v_cvt_pk_bf16_f32 v147, v154, v155
	s_nop 1
	v_permlane32_swap_b32_e32 v140, v142
	v_permlane32_swap_b32_e32 v141, v143
	v_permlane32_swap_b32_e32 v144, v146
	v_permlane32_swap_b32_e32 v145, v147
	v_exp_f32_e32 v156, v68
	v_exp_f32_e32 v157, v69
	v_exp_f32_e32 v158, v70
	v_exp_f32_e32 v159, v71
	v_exp_f32_e32 v160, v72
	v_exp_f32_e32 v161, v73
	v_exp_f32_e32 v162, v74
	v_exp_f32_e32 v163, v75
	v_exp_f32_e32 v164, v76
	v_exp_f32_e32 v165, v77
	v_exp_f32_e32 v166, v78
	v_exp_f32_e32 v167, v79
	v_exp_f32_e32 v168, v80
	v_exp_f32_e32 v169, v81
	v_exp_f32_e32 v170, v82
	v_exp_f32_e32 v171, v83
	v_add_f32_e32 v249, v156, v157
	v_add_f32_e32 v250, v158, v159
	v_add_f32_e32 v249, v249, v160
	v_add_f32_e32 v250, v250, v161
	v_add_f32_e32 v249, v249, v162
	v_add_f32_e32 v250, v250, v163
	v_add_f32_e32 v249, v249, v164
	v_add_f32_e32 v250, v250, v165
	v_add_f32_e32 v249, v249, v166
	v_add_f32_e32 v250, v250, v167
	v_add_f32_e32 v249, v249, v168
	v_add_f32_e32 v250, v250, v169
	v_add_f32_e32 v249, v249, v170
	v_add_f32_e32 v250, v250, v171
	v_add_f32_e32 v249, v249, v250
	v_cvt_pk_bf16_f32 v156, v156, v157
	v_cvt_pk_bf16_f32 v157, v158, v159
	v_cvt_pk_bf16_f32 v158, v160, v161
	v_cvt_pk_bf16_f32 v159, v162, v163
	v_cvt_pk_bf16_f32 v160, v164, v165
	v_cvt_pk_bf16_f32 v161, v166, v167
	v_cvt_pk_bf16_f32 v162, v168, v169
	v_cvt_pk_bf16_f32 v163, v170, v171
	s_nop 1
	v_permlane32_swap_b32_e32 v156, v158
	v_permlane32_swap_b32_e32 v157, v159
	v_permlane32_swap_b32_e32 v160, v162
	v_permlane32_swap_b32_e32 v161, v163
	s_branch .Lsum_a1b0

.Lsum_a1b0:
	v_add_f32_e32 v248, v248, v249
	v_cmp_gt_f32_e32 vcc, 0x5f800000, v248
	s_cmp_eq_u64 vcc, exec
	s_cbranch_scc0 .Lfb_a1b0
	v_mov_b32_e32 v249, v248
	s_nop 1
	v_permlane32_swap_b32_e32 v248, v249
	v_add_f32_e32 v248, v248, v249
	v_add_f32_e32 v191, v248, v191
	v_mov_b32_e32 v192, v193
	s_setprio 3
	s_waitcnt lgkmcnt(6)
	v_mfma_f32_32x32x16_bf16 v[52:67], v[208:211], v[140:143], v[52:67]
	ds_read_b64_tr_b16 v[208:209], v174 offset:512
	ds_read_b64_tr_b16 v[210:211], v174 offset:2560
	s_waitcnt lgkmcnt(6)
	v_mfma_f32_32x32x16_bf16 v[52:67], v[212:215], v[144:147], v[52:67]
	ds_read_b64_tr_b16 v[212:213], v174 offset:4608
	ds_read_b64_tr_b16 v[214:215], v174 offset:6656
	s_waitcnt lgkmcnt(6)
	v_mfma_f32_32x32x16_bf16 v[52:67], v[216:219], v[156:159], v[52:67]
	ds_read_b64_tr_b16 v[216:217], v174 offset:8704
	ds_read_b64_tr_b16 v[218:219], v174 offset:10752
	s_waitcnt lgkmcnt(6)
	v_mfma_f32_32x32x16_bf16 v[52:67], v[220:223], v[160:163], v[52:67]
	ds_read_b64_tr_b16 v[220:221], v174 offset:12800
	ds_read_b64_tr_b16 v[222:223], v174 offset:14848
	s_waitcnt lgkmcnt(6)
	v_mfma_f32_32x32x16_bf16 v[36:51], v[208:211], v[140:143], v[36:51]
	ds_read_b64_tr_b16 v[208:209], v174 offset:1024
	ds_read_b64_tr_b16 v[210:211], v174 offset:3072
	s_waitcnt lgkmcnt(6)
	v_mfma_f32_32x32x16_bf16 v[36:51], v[212:215], v[144:147], v[36:51]
	ds_read_b64_tr_b16 v[212:213], v174 offset:5120
	ds_read_b64_tr_b16 v[214:215], v174 offset:7168
	s_waitcnt lgkmcnt(6)
	v_mfma_f32_32x32x16_bf16 v[36:51], v[216:219], v[156:159], v[36:51]
	ds_read_b64_tr_b16 v[216:217], v174 offset:9216
	ds_read_b64_tr_b16 v[218:219], v174 offset:11264
	s_waitcnt lgkmcnt(6)
	v_mfma_f32_32x32x16_bf16 v[36:51], v[220:223], v[160:163], v[36:51]
	ds_read_b64_tr_b16 v[220:221], v174 offset:13312
	ds_read_b64_tr_b16 v[222:223], v174 offset:15360
	s_waitcnt lgkmcnt(6)
	v_mfma_f32_32x32x16_bf16 v[20:35], v[208:211], v[140:143], v[20:35]
	ds_read_b64_tr_b16 v[208:209], v174 offset:1536
	ds_read_b64_tr_b16 v[210:211], v174 offset:3584
	s_waitcnt lgkmcnt(6)
	v_mfma_f32_32x32x16_bf16 v[20:35], v[212:215], v[144:147], v[20:35]
	ds_read_b64_tr_b16 v[212:213], v174 offset:5632
	ds_read_b64_tr_b16 v[214:215], v174 offset:7680
	s_waitcnt lgkmcnt(6)
	v_mfma_f32_32x32x16_bf16 v[20:35], v[216:219], v[156:159], v[20:35]
	ds_read_b64_tr_b16 v[216:217], v174 offset:9728
	ds_read_b64_tr_b16 v[218:219], v174 offset:11776
	s_waitcnt lgkmcnt(6)
	v_mfma_f32_32x32x16_bf16 v[20:35], v[220:223], v[160:163], v[20:35]
	ds_read_b64_tr_b16 v[220:221], v174 offset:13824
	ds_read_b64_tr_b16 v[222:223], v174 offset:15872
	s_waitcnt lgkmcnt(6)
	v_mfma_f32_32x32x16_bf16 v[4:19], v[208:211], v[140:143], v[4:19]
	s_waitcnt lgkmcnt(4)
	v_mfma_f32_32x32x16_bf16 v[4:19], v[212:215], v[144:147], v[4:19]
	s_waitcnt lgkmcnt(2)
	v_mfma_f32_32x32x16_bf16 v[4:19], v[216:219], v[156:159], v[4:19]
	s_waitcnt lgkmcnt(0)
	v_mfma_f32_32x32x16_bf16 v[4:19], v[220:223], v[160:163], v[4:19]
	s_setprio 0
	s_branch .Ltail2_a1b0

.LBB0_1467:
	s_add_i32 s98, s18, 64
	s_cmp_le_i32 s98, s40
	s_cbranch_scc0 .Lorig_a1b1
	s_setprio 3
	ds_read_b128 v[140:143], v177
	ds_read_b128 v[144:147], v177 offset:32
	ds_read_b128 v[148:151], v177 offset:64
	ds_read_b128 v[152:155], v177 offset:96
	ds_read_b128 v[208:211], v172 offset:49152
	ds_read_b128 v[212:215], v206 offset:49152
	ds_read_b128 v[216:219], v207 offset:49152
	ds_read_b128 v[220:223], v237 offset:49152
	ds_read_b128 v[224:227], v244 offset:49152
	ds_read_b128 v[228:231], v245 offset:49152
	ds_read_b128 v[232:235], v246 offset:49152
	ds_read_b128 v[238:241], v247 offset:49152
	ds_read_b128 v[156:159], v177 offset:128
	ds_read_b128 v[160:163], v177 offset:160
	ds_read_b128 v[164:167], v177 offset:192
	ds_read_b128 v[168:171], v177 offset:224
	s_waitcnt lgkmcnt(11)
	v_mfma_f32_32x32x16_bf16 v[84:99], v[208:211], v[100:103], v[140:155]
	ds_read_b128 v[208:211], v172 offset:57344
	s_waitcnt lgkmcnt(11)
	v_mfma_f32_32x32x16_bf16 v[84:99], v[212:215], v[104:107], v[84:99]
	ds_read_b128 v[212:215], v206 offset:57344
	s_waitcnt lgkmcnt(11)
	v_mfma_f32_32x32x16_bf16 v[84:99], v[216:219], v[108:111], v[84:99]
	ds_read_b128 v[216:219], v207 offset:57344
	s_waitcnt lgkmcnt(11)
	v_mfma_f32_32x32x16_bf16 v[84:99], v[220:223], v[112:115], v[84:99]
	ds_read_b128 v[220:223], v237 offset:57344
	s_waitcnt lgkmcnt(11)
	v_mfma_f32_32x32x16_bf16 v[84:99], v[224:227], v[116:119], v[84:99]
	ds_read_b128 v[224:227], v244 offset:57344
	s_waitcnt lgkmcnt(11)
	v_mfma_f32_32x32x16_bf16 v[84:99], v[228:231], v[120:123], v[84:99]
	ds_read_b128 v[228:231], v245 offset:57344
	s_waitcnt lgkmcnt(11)
	v_mfma_f32_32x32x16_bf16 v[84:99], v[232:235], v[124:127], v[84:99]
	ds_read_b128 v[232:235], v246 offset:57344
	s_waitcnt lgkmcnt(11)
	v_mfma_f32_32x32x16_bf16 v[84:99], v[238:241], v[128:131], v[84:99]
	ds_read_b128 v[238:241], v247 offset:57344
	s_waitcnt lgkmcnt(7)
	v_mfma_f32_32x32x16_bf16 v[68:83], v[208:211], v[100:103], v[156:171]
	s_waitcnt lgkmcnt(6)
	v_mfma_f32_32x32x16_bf16 v[68:83], v[212:215], v[104:107], v[68:83]
	s_waitcnt lgkmcnt(5)
	v_mfma_f32_32x32x16_bf16 v[68:83], v[216:219], v[108:111], v[68:83]
	s_waitcnt lgkmcnt(4)
	v_mfma_f32_32x32x16_bf16 v[68:83], v[220:223], v[112:115], v[68:83]
	s_waitcnt lgkmcnt(3)
	v_mfma_f32_32x32x16_bf16 v[68:83], v[224:227], v[116:119], v[68:83]
	s_waitcnt lgkmcnt(2)
	v_mfma_f32_32x32x16_bf16 v[68:83], v[228:231], v[120:123], v[68:83]
	s_waitcnt lgkmcnt(1)
	v_mfma_f32_32x32x16_bf16 v[68:83], v[232:235], v[124:127], v[68:83]
	s_waitcnt lgkmcnt(0)
	v_mfma_f32_32x32x16_bf16 v[68:83], v[238:241], v[128:131], v[68:83]
	ds_read_b64_tr_b16 v[208:209], v174 offset:16384
	ds_read_b64_tr_b16 v[210:211], v174 offset:18432
	ds_read_b64_tr_b16 v[212:213], v174 offset:20480
	ds_read_b64_tr_b16 v[214:215], v174 offset:22528
	ds_read_b64_tr_b16 v[216:217], v174 offset:24576
	ds_read_b64_tr_b16 v[218:219], v174 offset:26624
	ds_read_b64_tr_b16 v[220:221], v174 offset:28672
	ds_read_b64_tr_b16 v[222:223], v174 offset:30720
	s_setprio 0
	s_nop 7
	s_nop 3
	v_cmp_eq_f32_e32 vcc, 0, v192
	s_cmp_eq_u64 vcc, exec
	s_cbranch_scc0 .Lsub_a1b1
	v_exp_f32_e32 v140, v84
	v_exp_f32_e32 v141, v85
	v_exp_f32_e32 v142, v86
	v_exp_f32_e32 v143, v87
	v_exp_f32_e32 v144, v88
	v_exp_f32_e32 v145, v89
	v_exp_f32_e32 v146, v90
	v_exp_f32_e32 v147, v91
	v_exp_f32_e32 v148, v92
	v_exp_f32_e32 v149, v93
	v_exp_f32_e32 v150, v94
	v_exp_f32_e32 v151, v95
	v_exp_f32_e32 v152, v96
	v_exp_f32_e32 v153, v97
	v_exp_f32_e32 v154, v98
	v_exp_f32_e32 v155, v99
	v_add_f32_e32 v248, v140, v141
	v_add_f32_e32 v250, v142, v143
	v_add_f32_e32 v248, v248, v144
	v_add_f32_e32 v250, v250, v145
	v_add_f32_e32 v248, v248, v146
	v_add_f32_e32 v250, v250, v147
	v_add_f32_e32 v248, v248, v148
	v_add_f32_e32 v250, v250, v149
	v_add_f32_e32 v248, v248, v150
	v_add_f32_e32 v250, v250, v151
	v_add_f32_e32 v248, v248, v152
	v_add_f32_e32 v250, v250, v153
	v_add_f32_e32 v248, v248, v154
	v_add_f32_e32 v250, v250, v155
	v_add_f32_e32 v248, v248, v250
	v_cvt_pk_bf16_f32 v140, v140, v141
	v_cvt_pk_bf16_f32 v141, v142, v143
	v_cvt_pk_bf16_f32 v142, v144, v145
	v_cvt_pk_bf16_f32 v143, v146, v147
	v_cvt_pk_bf16_f32 v144, v148, v149
	v_cvt_pk_bf16_f32 v145, v150, v151
	v_cvt_pk_bf16_f32 v146, v152, v153
	v_cvt_pk_bf16_f32 v147, v154, v155
	s_nop 1
	v_permlane32_swap_b32_e32 v140, v142
	v_permlane32_swap_b32_e32 v141, v143
	v_permlane32_swap_b32_e32 v144, v146
	v_permlane32_swap_b32_e32 v145, v147
	v_exp_f32_e32 v156, v68
	v_exp_f32_e32 v157, v69
	v_exp_f32_e32 v158, v70
	v_exp_f32_e32 v159, v71
	v_exp_f32_e32 v160, v72
	v_exp_f32_e32 v161, v73
	v_exp_f32_e32 v162, v74
	v_exp_f32_e32 v163, v75
	v_exp_f32_e32 v164, v76
	v_exp_f32_e32 v165, v77
	v_exp_f32_e32 v166, v78
	v_exp_f32_e32 v167, v79
	v_exp_f32_e32 v168, v80
	v_exp_f32_e32 v169, v81
	v_exp_f32_e32 v170, v82
	v_exp_f32_e32 v171, v83
	v_add_f32_e32 v249, v156, v157
	v_add_f32_e32 v250, v158, v159
	v_add_f32_e32 v249, v249, v160
	v_add_f32_e32 v250, v250, v161
	v_add_f32_e32 v249, v249, v162
	v_add_f32_e32 v250, v250, v163
	v_add_f32_e32 v249, v249, v164
	v_add_f32_e32 v250, v250, v165
	v_add_f32_e32 v249, v249, v166
	v_add_f32_e32 v250, v250, v167
	v_add_f32_e32 v249, v249, v168
	v_add_f32_e32 v250, v250, v169
	v_add_f32_e32 v249, v249, v170
	v_add_f32_e32 v250, v250, v171
	v_add_f32_e32 v249, v249, v250
	v_cvt_pk_bf16_f32 v156, v156, v157
	v_cvt_pk_bf16_f32 v157, v158, v159
	v_cvt_pk_bf16_f32 v158, v160, v161
	v_cvt_pk_bf16_f32 v159, v162, v163
	v_cvt_pk_bf16_f32 v160, v164, v165
	v_cvt_pk_bf16_f32 v161, v166, v167
	v_cvt_pk_bf16_f32 v162, v168, v169
	v_cvt_pk_bf16_f32 v163, v170, v171
	s_nop 1
	v_permlane32_swap_b32_e32 v156, v158
	v_permlane32_swap_b32_e32 v157, v159
	v_permlane32_swap_b32_e32 v160, v162
	v_permlane32_swap_b32_e32 v161, v163
	s_branch .Lsum_a1b1

.Lsum_a1b1:
	v_add_f32_e32 v248, v248, v249
	v_cmp_gt_f32_e32 vcc, 0x5f800000, v248
	s_cmp_eq_u64 vcc, exec
	s_cbranch_scc0 .Lfb_a1b1
	v_mov_b32_e32 v249, v248
	s_nop 1
	v_permlane32_swap_b32_e32 v248, v249
	v_add_f32_e32 v248, v248, v249
	v_add_f32_e32 v191, v248, v191
	v_mov_b32_e32 v193, v192
	s_setprio 3
	s_waitcnt lgkmcnt(6)
	v_mfma_f32_32x32x16_bf16 v[52:67], v[208:211], v[140:143], v[52:67]
	ds_read_b64_tr_b16 v[208:209], v174 offset:16896
	ds_read_b64_tr_b16 v[210:211], v174 offset:18944
	s_waitcnt lgkmcnt(6)
	v_mfma_f32_32x32x16_bf16 v[52:67], v[212:215], v[144:147], v[52:67]
	ds_read_b64_tr_b16 v[212:213], v174 offset:20992
	ds_read_b64_tr_b16 v[214:215], v174 offset:23040
	s_waitcnt lgkmcnt(6)
	v_mfma_f32_32x32x16_bf16 v[52:67], v[216:219], v[156:159], v[52:67]
	ds_read_b64_tr_b16 v[216:217], v174 offset:25088
	ds_read_b64_tr_b16 v[218:219], v174 offset:27136
	s_waitcnt lgkmcnt(6)
	v_mfma_f32_32x32x16_bf16 v[52:67], v[220:223], v[160:163], v[52:67]
	ds_read_b64_tr_b16 v[220:221], v174 offset:29184
	ds_read_b64_tr_b16 v[222:223], v174 offset:31232
	s_waitcnt lgkmcnt(6)
	v_mfma_f32_32x32x16_bf16 v[36:51], v[208:211], v[140:143], v[36:51]
	ds_read_b64_tr_b16 v[208:209], v174 offset:17408
	ds_read_b64_tr_b16 v[210:211], v174 offset:19456
	s_waitcnt lgkmcnt(6)
	v_mfma_f32_32x32x16_bf16 v[36:51], v[212:215], v[144:147], v[36:51]
	ds_read_b64_tr_b16 v[212:213], v174 offset:21504
	ds_read_b64_tr_b16 v[214:215], v174 offset:23552
	s_waitcnt lgkmcnt(6)
	v_mfma_f32_32x32x16_bf16 v[36:51], v[216:219], v[156:159], v[36:51]
	ds_read_b64_tr_b16 v[216:217], v174 offset:25600
	ds_read_b64_tr_b16 v[218:219], v174 offset:27648
	s_waitcnt lgkmcnt(6)
	v_mfma_f32_32x32x16_bf16 v[36:51], v[220:223], v[160:163], v[36:51]
	ds_read_b64_tr_b16 v[220:221], v174 offset:29696
	ds_read_b64_tr_b16 v[222:223], v174 offset:31744
	s_waitcnt lgkmcnt(6)
	v_mfma_f32_32x32x16_bf16 v[20:35], v[208:211], v[140:143], v[20:35]
	ds_read_b64_tr_b16 v[208:209], v174 offset:17920
	ds_read_b64_tr_b16 v[210:211], v174 offset:19968
	s_waitcnt lgkmcnt(6)
	v_mfma_f32_32x32x16_bf16 v[20:35], v[212:215], v[144:147], v[20:35]
	ds_read_b64_tr_b16 v[212:213], v174 offset:22016
	ds_read_b64_tr_b16 v[214:215], v174 offset:24064
	s_waitcnt lgkmcnt(6)
	v_mfma_f32_32x32x16_bf16 v[20:35], v[216:219], v[156:159], v[20:35]
	ds_read_b64_tr_b16 v[216:217], v174 offset:26112
	ds_read_b64_tr_b16 v[218:219], v174 offset:28160
	s_waitcnt lgkmcnt(6)
	v_mfma_f32_32x32x16_bf16 v[20:35], v[220:223], v[160:163], v[20:35]
	ds_read_b64_tr_b16 v[220:221], v174 offset:30208
	ds_read_b64_tr_b16 v[222:223], v174 offset:32256
	s_waitcnt lgkmcnt(6)
	v_mfma_f32_32x32x16_bf16 v[4:19], v[208:211], v[140:143], v[4:19]
	s_waitcnt lgkmcnt(4)
	v_mfma_f32_32x32x16_bf16 v[4:19], v[212:215], v[144:147], v[4:19]
	s_waitcnt lgkmcnt(2)
	v_mfma_f32_32x32x16_bf16 v[4:19], v[216:219], v[156:159], v[4:19]
	s_waitcnt lgkmcnt(0)
	v_mfma_f32_32x32x16_bf16 v[4:19], v[220:223], v[160:163], v[4:19]
	s_setprio 0
	s_branch .Ltail2_a1b1
